# waves 0-3 (K/V DMA issuers) at s_setprio 1 during the differential-attention runs
# baseline (speedup 1.0000x reference)
.LBB0_1201:
	v_cvt_pk_fp8_f32 v162, v98, v99
	v_cvt_pk_fp8_f32 v163, v102, v103
	v_cvt_pk_fp8_f32 v164, v106, v107
	v_cvt_pk_fp8_f32 v165, v110, v111
	v_cvt_pk_fp8_f32 v166, v82, v83
	v_cvt_pk_fp8_f32 v167, v86, v87
	v_cvt_pk_fp8_f32 v168, v90, v91
	v_cvt_pk_fp8_f32 v169, v94, v95
	v_cvt_pk_fp8_f32 v162, v100, v101 op_sel:[0,0,1]
	v_cvt_pk_fp8_f32 v163, v104, v105 op_sel:[0,0,1]
	v_cvt_pk_fp8_f32 v164, v108, v109 op_sel:[0,0,1]
	v_cvt_pk_fp8_f32 v165, v112, v113 op_sel:[0,0,1]
	v_cvt_pk_fp8_f32 v166, v84, v85 op_sel:[0,0,1]
	v_cvt_pk_fp8_f32 v167, v88, v89 op_sel:[0,0,1]
	v_cvt_pk_fp8_f32 v168, v92, v93 op_sel:[0,0,1]
	v_cvt_pk_fp8_f32 v169, v96, v97 op_sel:[0,0,1]
	s_waitcnt vmcnt(0) lgkmcnt(0)
	s_barrier
	ds_read_b128 v[82:85], v194 offset:0
	ds_read_b128 v[86:89], v195 offset:0
	ds_read_b128 v[90:93], v194 offset:0x800
	ds_read_b128 v[94:97], v195 offset:0x800
	s_nop 1
	v_mfma_f32_16x16x128_f8f6f4 v[18:21], v[162:169], v[146:153], v[18:21]
	ds_read_b128 v[98:101], v194 offset:0x1000
	ds_read_b128 v[102:105], v195 offset:0x1000
	s_waitcnt lgkmcnt(4)
	v_mfma_f32_32x32x64_f8f6f4 v[2:17], v[162:169], v[82:89], v[2:17]
	s_waitcnt lgkmcnt(2)
	v_mfma_f32_32x32x64_f8f6f4 v[34:49], v[162:169], v[90:97], v[34:49]
	s_nop 7
	s_nop 7
	ds_read_b128 v[82:85], v194 offset:0x1800
	ds_read_b128 v[86:89], v195 offset:0x1800
	s_waitcnt lgkmcnt(2)
	v_mfma_f32_32x32x64_f8f6f4 v[50:65], v[162:169], v[98:105], v[50:65]
	s_waitcnt lgkmcnt(0)
	v_mfma_f32_32x32x64_f8f6f4 v[66:81], v[162:169], v[82:89], v[66:81]
	s_setprio 0

.LBB0_1264:
	s_lshl_b32 s94, s77, 8
	s_add_i32 s77, s94, 0x8000
	s_and_b64 vcc, exec, s[38:39]
	s_cbranch_vccz .LBB0_1317
	s_setprio 1
	ds_read_b128 v[18:21], v183 offset:0
	ds_read_b128 v[22:25], v190 offset:0
	ds_read_b128 v[34:37], v183 offset:0x800
	ds_read_b128 v[38:41], v190 offset:0x800
	s_waitcnt lgkmcnt(0)
	s_waitcnt vmcnt(0)
	s_nop 9
	v_mfma_f32_32x32x64_f8f6f4 v[18:33], v[18:25], v[154:161], 0
	s_mov_b32 s37, s36
	s_mov_b32 s38, s36
	s_mov_b32 s39, s36
	s_mov_b32 s40, s36
	s_mov_b32 s41, s36
	s_mov_b32 s42, s36
	s_mov_b32 s43, s36
	s_mov_b32 s44, s36
	s_mov_b32 s45, s36
	s_mov_b32 s46, s36
	s_mov_b32 s47, s36
	s_mov_b32 s48, s36
	s_mov_b32 s49, s36
	s_mov_b32 s50, s36
	s_mov_b32 s51, s36
	v_mov_b64_e32 v[2:3], s[36:37]
	v_mov_b64_e32 v[4:5], s[38:39]
	v_mov_b64_e32 v[6:7], s[40:41]
	v_mov_b64_e32 v[8:9], s[42:43]
	v_mov_b64_e32 v[10:11], s[44:45]
	v_mov_b64_e32 v[12:13], s[46:47]
	v_mov_b64_e32 v[14:15], s[48:49]
	v_mov_b64_e32 v[16:17], s[50:51]
	v_max_f32_e32 v42, v19, v19
	v_max_f32_e32 v43, v18, v18
	v_max_f32_e32 v42, v43, v42
	v_max3_f32 v42, v42, v20, v21
	v_max3_f32 v42, v42, v22, v23
	v_max3_f32 v42, v42, v24, v25
	v_max3_f32 v42, v42, v26, v27
	v_max3_f32 v42, v42, v28, v29
	v_max3_f32 v50, v42, v30, v31
	v_mfma_f32_32x32x64_f8f6f4 v[34:49], v[34:41], v[154:161], 0
	v_max3_f32 v50, v50, v32, v33
	s_lshl_b32 s45, s81, 10
	s_lshl_b32 s46, s80, 10
	s_cmp_lg_u32 0, -1
	s_cselect_b32 s38, 0, 0
	s_add_i32 s37, s38, 0x2000
	s_add_i32 s39, s38, 0x3000
	s_add_i32 s6, s38, 0x1000
	v_add_u32_e32 v203, s37, v194
	s_add_i32 s37, s38, 0x6000
	v_add_u32_e32 v199, s39, v194
	s_add_i32 s39, s38, 0x8000
	s_add_i32 s38, s38, 0xa000
	v_add_u32_e32 v205, s6, v194
	v_add_u32_e32 v201, s37, v194
	s_nop 4
	v_max3_f32 v50, v50, v34, v35
	v_max3_f32 v50, v50, v36, v37
	v_max3_f32 v50, v50, v38, v39
	v_max3_f32 v50, v50, v40, v41
	v_max3_f32 v50, v50, v42, v43
	v_max3_f32 v50, v50, v44, v45
	v_max3_f32 v50, v50, v46, v47
	v_max3_f32 v50, v50, v48, v49
	v_mov_b32_e32 v51, v50
	s_nop 1
	v_permlane32_swap_b32_e32 v50, v51
	v_max_f32_e32 v51, v51, v51
	v_max_f32_e32 v50, v50, v50
	v_max_f32_e32 v50, v50, v51
	s_cmp_eq_u32 s98, 0
	s_cselect_b32 s100, 0x40000000, 0xc0600000
	v_add_f32_e32 v198, s100, v50
	v_add_u32_e32 v196, s39, v194
	v_add_u32_e32 v194, s38, v194
	s_lshl_b32 s38, s95, 4
	v_sub_f32_e32 v18, v18, v198
	s_and_b32 s38, s38, 0xfffffc00
	s_ashr_i32 s89, s88, 31
	v_exp_f32_e32 v114, v18
	s_or_b32 s40, s88, 0x100
	s_add_i32 s41, s94, 0x4100
	s_or_b32 s42, s88, 0x140
	s_add_i32 s43, s94, 0x4140
	v_lshl_or_b32 v18, v193, 4, s38
	s_lshl_b64 s[38:39], s[88:89], 10
	s_add_u32 s38, s38, s87
	v_xor_b32_e32 v82, 0x80000000, v198
	v_sub_f32_e32 v34, v34, v198
	v_sub_f32_e32 v19, v19, v198
	v_sub_f32_e32 v35, v35, v198
	v_sub_f32_e32 v20, v20, v198
	v_sub_f32_e32 v36, v36, v198
	v_sub_f32_e32 v21, v21, v198
	v_sub_f32_e32 v37, v37, v198
	v_sub_f32_e32 v22, v22, v198
	v_sub_f32_e32 v38, v38, v198
	v_sub_f32_e32 v23, v23, v198
	v_sub_f32_e32 v39, v39, v198
	v_sub_f32_e32 v24, v24, v198
	v_sub_f32_e32 v40, v40, v198
	v_sub_f32_e32 v25, v25, v198
	v_sub_f32_e32 v41, v41, v198
	v_sub_f32_e32 v26, v26, v198
	v_sub_f32_e32 v42, v42, v198
	v_sub_f32_e32 v27, v27, v198
	v_sub_f32_e32 v43, v43, v198
	v_sub_f32_e32 v28, v28, v198
	v_sub_f32_e32 v44, v44, v198
	v_sub_f32_e32 v29, v29, v198
	v_sub_f32_e32 v45, v45, v198
	v_sub_f32_e32 v30, v30, v198
	v_sub_f32_e32 v46, v46, v198
	v_sub_f32_e32 v31, v31, v198
	v_sub_f32_e32 v47, v47, v198
	v_sub_f32_e32 v32, v32, v198
	v_sub_f32_e32 v48, v48, v198
	v_sub_f32_e32 v33, v33, v198
	v_sub_f32_e32 v49, v49, v198
	s_addc_u32 s39, s39, s76
	v_mov_b32_e32 v83, v82
	v_mov_b32_e32 v84, v82
	v_mov_b32_e32 v85, v82
	v_mov_b32_e32 v86, v82
	v_mov_b32_e32 v87, v82
	v_mov_b32_e32 v88, v82
	v_mov_b32_e32 v89, v82
	v_mov_b32_e32 v90, v82
	v_mov_b32_e32 v91, v82
	v_mov_b32_e32 v92, v82
	v_mov_b32_e32 v93, v82
	v_mov_b32_e32 v94, v82
	v_mov_b32_e32 v95, v82
	v_mov_b32_e32 v96, v82
	v_mov_b32_e32 v97, v82
	v_exp_f32_e32 v98, v34
	v_exp_f32_e32 v115, v19
	v_exp_f32_e32 v99, v35
	v_exp_f32_e32 v116, v20
	v_exp_f32_e32 v100, v36
	v_exp_f32_e32 v117, v21
	v_exp_f32_e32 v101, v37
	v_exp_f32_e32 v118, v22
	v_exp_f32_e32 v102, v38
	v_exp_f32_e32 v119, v23
	v_exp_f32_e32 v103, v39
	v_exp_f32_e32 v120, v24
	v_exp_f32_e32 v104, v40
	v_exp_f32_e32 v121, v25
	v_exp_f32_e32 v105, v41
	v_exp_f32_e32 v122, v26
	v_exp_f32_e32 v106, v42
	v_exp_f32_e32 v123, v27
	v_exp_f32_e32 v107, v43
	v_exp_f32_e32 v124, v28
	v_exp_f32_e32 v108, v44
	v_exp_f32_e32 v125, v29
	v_exp_f32_e32 v109, v45
	v_exp_f32_e32 v126, v30
	v_exp_f32_e32 v110, v46
	v_exp_f32_e32 v127, v31
	v_exp_f32_e32 v111, v47
	v_exp_f32_e32 v128, v32
	v_exp_f32_e32 v112, v48
	v_exp_f32_e32 v129, v33
	v_exp_f32_e32 v113, v49
	v_mov_b32_e32 v19, v181
	s_add_u32 s38, s38, 0x29c30000
	s_waitcnt vmcnt(3) lgkmcnt(0)
	s_barrier
	v_lshl_add_u64 v[172:173], s[92:93], 0, v[18:19]
	s_addc_u32 s39, s39, 0
	v_add3_u32 v18, s79, v191, v192
	v_lshl_add_u64 v[174:175], s[38:39], 0, v[18:19]
	v_mov_b32_e32 v162, 0
	v_mov_b64_e32 v[48:49], v[16:17]
	v_mov_b64_e32 v[64:65], v[16:17]
	v_mov_b64_e32 v[80:81], v[16:17]
	v_mov_b64_e32 v[32:33], v[16:17]
	v_lshl_add_u64 v[170:171], s[28:29], 0, v[180:181]
	v_add_u32_e32 v206, v205, v195
	v_cmp_gt_u32_e64 s[6:7], 32, v193
	v_add_u32_e32 v204, v203, v195
	v_add_u32_e32 v202, v201, v195
	s_movk_i32 s37, 0x100
	v_add_u32_e32 v200, v199, v195
	v_add_u32_e32 v197, v196, v195
	v_add_u32_e32 v195, v194, v195
	s_mov_b32 s44, -3
	s_add_i32 s45, s45, 0
	s_add_i32 s46, s46, 0
	v_mov_b64_e32 v[46:47], v[14:15]
	v_mov_b64_e32 v[44:45], v[12:13]
	v_mov_b64_e32 v[42:43], v[10:11]
	v_mov_b64_e32 v[40:41], v[8:9]
	v_mov_b64_e32 v[38:39], v[6:7]
	v_mov_b64_e32 v[36:37], v[4:5]
	v_mov_b64_e32 v[34:35], v[2:3]
	v_mov_b64_e32 v[62:63], v[14:15]
	v_mov_b64_e32 v[60:61], v[12:13]
	v_mov_b64_e32 v[58:59], v[10:11]
	v_mov_b64_e32 v[56:57], v[8:9]
	v_mov_b64_e32 v[54:55], v[6:7]
	v_mov_b64_e32 v[52:53], v[4:5]
	v_mov_b64_e32 v[50:51], v[2:3]
	v_mov_b64_e32 v[78:79], v[14:15]
	v_mov_b64_e32 v[76:77], v[12:13]
	v_mov_b64_e32 v[74:75], v[10:11]
	v_mov_b64_e32 v[72:73], v[8:9]
	v_mov_b64_e32 v[70:71], v[6:7]
	v_mov_b64_e32 v[68:69], v[4:5]
	v_mov_b64_e32 v[66:67], v[2:3]
	v_mov_b64_e32 v[30:31], v[14:15]
	v_mov_b64_e32 v[28:29], v[12:13]
	v_mov_b64_e32 v[26:27], v[10:11]
	v_mov_b64_e32 v[24:25], v[8:9]
	v_mov_b64_e32 v[22:23], v[6:7]
	v_mov_b64_e32 v[20:21], v[4:5]
	v_mov_b64_e32 v[18:19], v[2:3]
	v_mov_b32_e32 v163, v162
	v_mov_b32_e32 v164, v162
	v_mov_b32_e32 v165, v162
	v_mov_b32_e32 v166, v162
	v_mov_b32_e32 v167, v162
	v_mov_b32_e32 v168, v162
	v_mov_b32_e32 v169, v162
	s_cmp_lg_u32 s98, 0
	s_cbranch_scc1 .LBB0_1268
	s_branch .Lf_1268

.LBB0_1376:
	s_and_b64 vcc, exec, s[38:39]
	s_cbranch_vccz .LBB0_1202
	s_setprio 1
	ds_read_b128 v[18:21], v183 offset:0
	ds_read_b128 v[22:25], v190 offset:0
	ds_read_b128 v[34:37], v183 offset:0x800
	ds_read_b128 v[38:41], v190 offset:0x800
	s_waitcnt lgkmcnt(0)
	s_waitcnt vmcnt(0)
	s_nop 11
	v_mfma_f32_32x32x64_f8f6f4 v[18:33], v[18:25], v[154:161], 0
	s_mov_b32 s37, s36
	s_mov_b32 s38, s36
	s_mov_b32 s39, s36
	s_mov_b32 s40, s36
	s_mov_b32 s41, s36
	s_mov_b32 s42, s36
	s_mov_b32 s43, s36
	s_mov_b32 s44, s36
	s_mov_b32 s45, s36
	s_mov_b32 s46, s36
	s_mov_b32 s47, s36
	s_mov_b32 s48, s36
	s_mov_b32 s49, s36
	s_mov_b32 s50, s36
	s_mov_b32 s51, s36
	v_mov_b64_e32 v[2:3], s[36:37]
	v_mov_b64_e32 v[4:5], s[38:39]
	v_mov_b64_e32 v[6:7], s[40:41]
	v_mov_b64_e32 v[8:9], s[42:43]
	v_mov_b64_e32 v[10:11], s[44:45]
	v_mov_b64_e32 v[12:13], s[46:47]
	v_mov_b64_e32 v[14:15], s[48:49]
	v_mov_b64_e32 v[16:17], s[50:51]
	v_max_f32_e32 v42, v19, v19
	v_max_f32_e32 v43, v18, v18
	v_max_f32_e32 v42, v43, v42
	v_max3_f32 v42, v42, v20, v21
	v_max3_f32 v42, v42, v22, v23
	v_max3_f32 v42, v42, v24, v25
	v_max3_f32 v42, v42, v26, v27
	v_max3_f32 v42, v42, v28, v29
	v_max3_f32 v50, v42, v30, v31
	v_mfma_f32_32x32x64_f8f6f4 v[34:49], v[34:41], v[154:161], 0
	v_max3_f32 v50, v50, v32, v33
	s_lshl_b32 s45, s95, 10
	s_lshl_b32 s46, s81, 10
	s_cmp_lg_u32 0, -1
	s_cselect_b32 s38, 0, 0
	s_add_i32 s37, s38, 0x2000
	s_add_i32 s39, s38, 0x3000
	s_add_i32 s6, s38, 0x1000
	v_add_u32_e32 v203, s37, v194
	s_add_i32 s37, s38, 0x6000
	v_add_u32_e32 v199, s39, v194
	s_add_i32 s39, s38, 0x8000
	s_add_i32 s38, s38, 0xa000
	v_add_u32_e32 v205, s6, v194
	v_add_u32_e32 v201, s37, v194
	s_nop 4
	v_max3_f32 v50, v50, v34, v35
	v_max3_f32 v50, v50, v36, v37
	v_max3_f32 v50, v50, v38, v39
	v_max3_f32 v50, v50, v40, v41
	v_max3_f32 v50, v50, v42, v43
	v_max3_f32 v50, v50, v44, v45
	v_max3_f32 v50, v50, v46, v47
	v_max3_f32 v50, v50, v48, v49
	v_mov_b32_e32 v51, v50
	s_nop 1
	v_permlane32_swap_b32_e32 v50, v51
	v_max_f32_e32 v51, v51, v51
	v_max_f32_e32 v50, v50, v50
	v_max_f32_e32 v50, v50, v51
	s_cmp_eq_u32 s98, 0
	s_cselect_b32 s100, 0x40000000, 0xc0600000
	v_add_f32_e32 v198, s100, v50
	v_sub_f32_e32 v18, v18, v198
	v_sub_f32_e32 v19, v19, v198
	v_add_u32_e32 v196, s39, v194
	v_add_u32_e32 v194, s38, v194
	s_lshl_b32 s38, s80, 4
	v_exp_f32_e32 v114, v18
	v_exp_f32_e32 v115, v19
	v_lshl_add_u64 v[18:19], s[16:17], 0, v[180:181]
	s_and_b32 s38, s38, 0xfffffc00
	s_ashr_i32 s89, s88, 31
	s_or_b32 s40, s88, 0x100
	s_add_i32 s41, s94, 0x4100
	s_or_b32 s42, s88, 0x140
	s_add_i32 s43, s94, 0x4140
	v_lshl_add_u64 v[170:171], v[18:19], 0, s[28:29]
	v_lshl_or_b32 v18, v193, 4, s38
	s_lshl_b64 s[38:39], s[88:89], 10
	s_add_u32 s38, s38, s87
	v_xor_b32_e32 v82, 0x80000000, v198
	v_sub_f32_e32 v34, v34, v198
	v_sub_f32_e32 v35, v35, v198
	v_sub_f32_e32 v20, v20, v198
	v_sub_f32_e32 v36, v36, v198
	v_sub_f32_e32 v21, v21, v198
	v_sub_f32_e32 v37, v37, v198
	v_sub_f32_e32 v22, v22, v198
	v_sub_f32_e32 v38, v38, v198
	v_sub_f32_e32 v23, v23, v198
	v_sub_f32_e32 v39, v39, v198
	v_sub_f32_e32 v24, v24, v198
	v_sub_f32_e32 v40, v40, v198
	v_sub_f32_e32 v25, v25, v198
	v_sub_f32_e32 v41, v41, v198
	v_sub_f32_e32 v26, v26, v198
	v_sub_f32_e32 v42, v42, v198
	v_sub_f32_e32 v27, v27, v198
	v_sub_f32_e32 v43, v43, v198
	v_sub_f32_e32 v28, v28, v198
	v_sub_f32_e32 v44, v44, v198
	v_sub_f32_e32 v29, v29, v198
	v_sub_f32_e32 v45, v45, v198
	v_sub_f32_e32 v30, v30, v198
	v_sub_f32_e32 v46, v46, v198
	v_sub_f32_e32 v31, v31, v198
	v_sub_f32_e32 v47, v47, v198
	v_sub_f32_e32 v32, v32, v198
	v_sub_f32_e32 v48, v48, v198
	v_sub_f32_e32 v33, v33, v198
	v_sub_f32_e32 v49, v49, v198
	s_addc_u32 s39, s39, s76
	v_mov_b32_e32 v83, v82
	v_mov_b32_e32 v84, v82
	v_mov_b32_e32 v85, v82
	v_mov_b32_e32 v86, v82
	v_mov_b32_e32 v87, v82
	v_mov_b32_e32 v88, v82
	v_mov_b32_e32 v89, v82
	v_mov_b32_e32 v90, v82
	v_mov_b32_e32 v91, v82
	v_mov_b32_e32 v92, v82
	v_mov_b32_e32 v93, v82
	v_mov_b32_e32 v94, v82
	v_mov_b32_e32 v95, v82
	v_mov_b32_e32 v96, v82
	v_mov_b32_e32 v97, v82
	v_exp_f32_e32 v98, v34
	v_exp_f32_e32 v99, v35
	v_exp_f32_e32 v116, v20
	v_exp_f32_e32 v100, v36
	v_exp_f32_e32 v117, v21
	v_exp_f32_e32 v101, v37
	v_exp_f32_e32 v118, v22
	v_exp_f32_e32 v102, v38
	v_exp_f32_e32 v119, v23
	v_exp_f32_e32 v103, v39
	v_exp_f32_e32 v120, v24
	v_exp_f32_e32 v104, v40
	v_exp_f32_e32 v121, v25
	v_exp_f32_e32 v105, v41
	v_exp_f32_e32 v122, v26
	v_exp_f32_e32 v106, v42
	v_exp_f32_e32 v123, v27
	v_exp_f32_e32 v107, v43
	v_exp_f32_e32 v124, v28
	v_exp_f32_e32 v108, v44
	v_exp_f32_e32 v125, v29
	v_exp_f32_e32 v109, v45
	v_exp_f32_e32 v126, v30
	v_exp_f32_e32 v110, v46
	v_exp_f32_e32 v127, v31
	v_exp_f32_e32 v111, v47
	v_exp_f32_e32 v128, v32
	v_exp_f32_e32 v112, v48
	v_exp_f32_e32 v129, v33
	v_exp_f32_e32 v113, v49
	v_mov_b32_e32 v19, v181
	s_add_u32 s38, s38, 0x29c30040
	s_waitcnt vmcnt(3) lgkmcnt(0)
	s_barrier
	v_lshl_add_u64 v[172:173], s[92:93], 0, v[18:19]
	s_addc_u32 s39, s39, 0
	v_add3_u32 v18, s79, v191, v192
	v_lshl_add_u64 v[174:175], s[38:39], 0, v[18:19]
	v_mov_b32_e32 v162, 0
	v_mov_b64_e32 v[48:49], v[16:17]
	v_mov_b64_e32 v[64:65], v[16:17]
	v_mov_b64_e32 v[80:81], v[16:17]
	v_mov_b64_e32 v[32:33], v[16:17]
	v_add_u32_e32 v206, v205, v195
	v_cmp_gt_u32_e64 s[6:7], 32, v193
	v_add_u32_e32 v204, v203, v195
	v_add_u32_e32 v202, v201, v195
	s_movk_i32 s37, 0x100
	v_add_u32_e32 v200, v199, v195
	v_add_u32_e32 v197, v196, v195
	v_add_u32_e32 v195, v194, v195
	s_mov_b32 s44, -3
	s_add_i32 s45, s45, 0
	s_add_i32 s46, s46, 0
	v_mov_b64_e32 v[46:47], v[14:15]
	v_mov_b64_e32 v[44:45], v[12:13]
	v_mov_b64_e32 v[42:43], v[10:11]
	v_mov_b64_e32 v[40:41], v[8:9]
	v_mov_b64_e32 v[38:39], v[6:7]
	v_mov_b64_e32 v[36:37], v[4:5]
	v_mov_b64_e32 v[34:35], v[2:3]
	v_mov_b64_e32 v[62:63], v[14:15]
	v_mov_b64_e32 v[60:61], v[12:13]
	v_mov_b64_e32 v[58:59], v[10:11]
	v_mov_b64_e32 v[56:57], v[8:9]
	v_mov_b64_e32 v[54:55], v[6:7]
	v_mov_b64_e32 v[52:53], v[4:5]
	v_mov_b64_e32 v[50:51], v[2:3]
	v_mov_b64_e32 v[78:79], v[14:15]
	v_mov_b64_e32 v[76:77], v[12:13]
	v_mov_b64_e32 v[74:75], v[10:11]
	v_mov_b64_e32 v[72:73], v[8:9]
	v_mov_b64_e32 v[70:71], v[6:7]
	v_mov_b64_e32 v[68:69], v[4:5]
	v_mov_b64_e32 v[66:67], v[2:3]
	v_mov_b64_e32 v[30:31], v[14:15]
	v_mov_b64_e32 v[28:29], v[12:13]
	v_mov_b64_e32 v[26:27], v[10:11]
	v_mov_b64_e32 v[24:25], v[8:9]
	v_mov_b64_e32 v[22:23], v[6:7]
	v_mov_b64_e32 v[20:21], v[4:5]
	v_mov_b64_e32 v[18:19], v[2:3]
	v_mov_b32_e32 v163, v162
	v_mov_b32_e32 v164, v162
	v_mov_b32_e32 v165, v162
	v_mov_b32_e32 v166, v162
	v_mov_b32_e32 v167, v162
	v_mov_b32_e32 v168, v162
	v_mov_b32_e32 v169, v162
	s_cmp_lg_u32 s98, 0
	s_cbranch_scc1 .LBB0_1380
	s_branch .Lf_1380
